# T10 variant: 14336 items moved, waves 1..7, one unit per wave per seam, last fill seam 14
# speedup vs baseline: 1.0072x; 1.0006x over previous
; __device__ __forceinline__ void transpose_item_f8(const float* W, int N, unsigned char* WT, int ldt, int kind, int off, int item, int lane, float scale) {
;     const int nblk = N >> 6, kb = item / nblk, nb = item - kb * nblk, k0 = 128 * kb + 16 * (lane & 7), n = 64 * nb + 4 * (lane >> 3);
;     const f32x4* src = (const f32x4*)(W + (size_t)k0 * N + n);
;     f32x4 v[2][16];
; #pragma unroll
;     for (int hh = 0; hh < 2; ++hh)
; #pragma unroll
;         for (int j = 0; j < 16; ++j) v[hh][j] = __builtin_nontemporal_load(src + (size_t)j * (N >> 2) + 8 * hh);
; #pragma unroll
;     for (int hh = 0; hh < 2; ++hh)
; #pragma unroll
;         for (int i = 0; i < 4; ++i) { v4u o; o.x = pg8::pk4_fp8(v[hh][0][i] * scale, v[hh][1][i] * scale, v[hh][2][i] * scale, v[hh][3][i] * scale); o.y = pg8::pk4_fp8(v[hh][4][i] * scale, v[hh][5][i] * scale, v[hh][6][i] * scale, v[hh][7][i] * scale);
;             o.z = pg8::pk4_fp8(v[hh][8][i] * scale, v[hh][9][i] * scale, v[hh][10][i] * scale, v[hh][11][i] * scale); o.w = pg8::pk4_fp8(v[hh][12][i] * scale, v[hh][13][i] * scale, v[hh][14][i] * scale, v[hh][15][i] * scale);
;             __builtin_nontemporal_store(o, (v4u*)(WT + (size_t)rowmap(kind, off, n + 32 * hh + i) * ldt + k0)); }
; __device__ __forceinline__ void moe_convert(Frame& F, int lo, int hi, int rank, int nrank) {
;     ...
;     for (int it = lo + rank; it < hi; it += nrank) {
;         int r = it; const float* W; unsigned char* WT; int N, ldt, kind, off; float f8s;
;         if (r < 14336) { const int e = r / 1792; r -= e * 1792; W = F.in[IN_WMG] + (size_t)e * 2048 * DFFE; N = DFFE; WT = F.ws + WS_WGU1 + (size_t)e * 14336 * 2048; ldt = 2048; kind = 1; off = 0; f8s = 32.f; }
;         else if ((r -= 14336) < 14336) { const int e = r / 1792; r -= e * 1792; W = F.in[IN_WMU] + (size_t)e * 2048 * DFFE; N = DFFE; WT = F.ws + WS_WGU1 + (size_t)e * 14336 * 2048; ldt = 2048; kind = 1; off = 128; f8s = 256.f; }
;         else { r -= 14336; const int e = r / 1792; r -= e * 1792; W = F.in[IN_WMD] + (size_t)e * DFFE * 2048; N = 2048; WT = F.ws + WS_WDN1 + (size_t)e * 2048 * DFFE; ldt = DFFE; kind = 0; off = 0; f8s = 64.f; }
;         transpose_item_f8(W, N, WT, ldt, kind, off, r, F.lane, f8s);
.LBB0_235:
	s_cmp_gt_i32 s24, 0x4fff
	s_cbranch_scc1 .LBB0_246
	s_add_u32 s14, s86, 0x23800000
	s_addc_u32 s15, s87, 0
	v_lshlrev_b32_e32 v1, 4, v0
	s_waitcnt vmcnt(2)
	v_lshrrev_b32_e32 v2, 1, v0
	s_add_u32 s16, s86, 0x7800000
	v_and_b32_e32 v1, 0x70, v1
	v_and_b32_e32 v134, 28, v2
	s_addc_u32 s17, s87, 0
	s_add_i32 s18, s24, 0xffff9000
	s_mov_b32 s3, 0
	s_mov_b32 s19, 0xc3e00000
	v_mov_b32_e32 v135, 0x43e00000
	v_mov_b32_e32 v136, 0x5c
	s_movk_i32 s20, 0x5d
	s_movk_i32 s21, 0x5e
	s_movk_i32 s22, 0x5f
	s_movk_i32 s23, 0x7c
	s_movk_i32 s26, 0x7d
	s_movk_i32 s27, 0x7e
	s_movk_i32 s28, 0x7f
	s_mov_b32 s29, s24
	s_branch .LBB0_238
.LBB0_237:
	s_lshr_b32 s12, s2, 6
	v_cvt_f32_u32_e32 v2, s12
	s_sub_i32 s35, 0, s12
	s_abs_i32 s34, s33
	s_ashr_i32 s13, s33, 31
	v_rcp_iflag_f32_e32 v2, v2
	v_mov_b32_e32 v138, 0
	v_mov_b32_e32 v139, 0
	v_mov_b32_e32 v140, 0
	v_mul_f32_e32 v2, 0x4f7ffffe, v2
	v_cvt_u32_f32_e32 v2, v2
	v_mov_b32_e32 v141, 0
	v_readfirstlane_b32 s36, v2
	s_mul_i32 s35, s35, s36
	s_mul_hi_u32 s35, s36, s35
	s_add_i32 s36, s36, s35
	s_mul_hi_u32 s35, s34, s36
	s_mul_i32 s36, s35, s12
	s_sub_i32 s34, s34, s36
	s_add_i32 s37, s35, 1
	s_sub_i32 s36, s34, s12
	s_cmp_ge_u32 s34, s12
	s_cselect_b32 s35, s37, s35
	s_cselect_b32 s34, s36, s34
	s_add_i32 s36, s35, 1
	s_cmp_ge_u32 s34, s12
	s_cselect_b32 s34, s36, s35
	s_xor_b32 s34, s34, s13
	s_sub_i32 s13, s34, s13
	v_lshl_or_b32 v132, s13, 7, v1
	s_mul_i32 s12, s13, s12
	v_mad_u64_u32 v[2:3], s[34:35], v132, s2, 0
	s_sub_i32 s12, s33, s12
	v_ashrrev_i32_e32 v133, 31, v132
	v_mov_b32_e32 v4, v3
	s_lshl_b32 s13, s12, 6
	v_mad_u64_u32 v[4:5], s[34:35], v133, s2, v[4:5]
	v_or_b32_e32 v130, s13, v134
	v_mov_b32_e32 v3, v4
	v_lshl_add_u64 v[2:3], v[2:3], 2, s[10:11]
	v_ashrrev_i32_e32 v131, 31, v130
	v_lshl_add_u64 v[2:3], v[130:131], 2, v[2:3]
	s_lshr_b32 s10, s2, 2
	s_mov_b32 s11, s3
	v_lshl_add_u64 v[4:5], s[10:11], 4, v[2:3]
	s_lshr_b32 s34, s2, 1
	s_mov_b32 s35, s3
	global_load_dwordx4 v[66:69], v[2:3], off nt
	global_load_dwordx4 v[70:73], v[4:5], off nt
	s_waitcnt vmcnt(2)
	v_lshl_add_u64 v[6:7], s[34:35], 4, v[2:3]
	s_mul_i32 s34, s10, 3
	s_mul_i32 s36, s10, 6
	s_mov_b32 s37, s3
	v_lshl_add_u64 v[8:9], s[34:35], 4, v[2:3]
	s_ashr_i32 s35, s2, 31
	s_mov_b32 s34, s2
	v_lshl_add_u64 v[12:13], s[36:37], 4, v[2:3]
	s_mul_i32 s36, s10, 7
	v_lshl_add_u64 v[10:11], s[2:3], 4, v[2:3]
	v_lshl_add_u64 v[14:15], s[36:37], 4, v[2:3]
	v_lshl_add_u64 v[16:17], s[34:35], 4, v[4:5]
	global_load_dwordx4 v[74:77], v[10:11], off nt
	global_load_dwordx4 v[90:93], v[12:13], off nt
	global_load_dwordx4 v[86:89], v[14:15], off nt
	global_load_dwordx4 v[102:105], v[16:17], off nt
	s_lshl_b32 s2, s2, 1
	global_load_dwordx4 v[82:85], v[6:7], off nt
	global_load_dwordx4 v[78:81], v[8:9], off nt
	v_lshl_add_u64 v[18:19], s[2:3], 4, v[2:3]
	s_mul_i32 s2, s10, 9
	v_lshl_add_u64 v[20:21], s[2:3], 4, v[2:3]
	global_load_dwordx4 v[94:97], v[18:19], off nt
	global_load_dwordx4 v[98:101], v[20:21], off nt
	s_mul_i32 s2, s10, 10
	v_lshl_add_u64 v[54:55], s[2:3], 4, v[2:3]
	s_mul_i32 s2, s10, 11
	v_lshl_add_u64 v[56:57], s[2:3], 4, v[2:3]
	s_mul_i32 s2, s10, 12
	global_load_dwordx4 v[114:117], v[54:55], off nt
	global_load_dwordx4 v[106:109], v[56:57], off nt
	v_lshl_add_u64 v[58:59], s[2:3], 4, v[2:3]
	s_mul_i32 s2, s10, 13
	v_lshl_add_u64 v[60:61], s[2:3], 4, v[2:3]
	global_load_dwordx4 v[110:113], v[58:59], off nt
	global_load_dwordx4 v[118:121], v[60:61], off nt
	s_mul_i32 s2, s10, 14
	v_lshl_add_u64 v[62:63], s[2:3], 4, v[2:3]
	s_mul_i32 s2, s10, 15
	v_lshl_add_u64 v[142:143], s[2:3], 4, v[2:3]
	global_load_dwordx4 v[122:125], v[62:63], off nt
	global_load_dwordx4 v[126:129], v[142:143], off nt
	global_load_dwordx4 v[42:45], v[2:3], off offset:128 nt
	global_load_dwordx4 v[46:49], v[4:5], off offset:128 nt
	global_load_dwordx4 v[50:53], v[6:7], off offset:128 nt
	global_load_dwordx4 v[38:41], v[8:9], off offset:128 nt
	global_load_dwordx4 v[30:33], v[10:11], off offset:128 nt
	global_load_dwordx4 v[26:29], v[12:13], off offset:128 nt
	global_load_dwordx4 v[22:25], v[14:15], off offset:128 nt
	global_load_dwordx4 v[34:37], v[16:17], off offset:128 nt
	s_nop 0
	global_load_dwordx4 v[10:13], v[18:19], off offset:128 nt
	global_load_dwordx4 v[14:17], v[20:21], off offset:128 nt
	s_nop 0
	global_load_dwordx4 v[18:21], v[54:55], off offset:128 nt
	global_load_dwordx4 v[6:9], v[56:57], off offset:128 nt
	global_load_dwordx4 v[2:5], v[58:59], off offset:128 nt
	s_lshl_b32 s2, s12, 7
	s_and_b32 s2, s2, 0xffffff00
	s_or_b32 s2, s2, s30
	v_lshl_add_u64 v[132:133], s[8:9], 0, v[132:133]
	s_add_i32 s29, s29, s25
	s_add_i32 s18, s18, s25
	s_cmp_lt_i32 s29, 0x5000
	s_waitcnt vmcnt(28)
	v_mul_f32_e32 v54, s31, v66
	s_waitcnt vmcnt(27)
	v_mul_f32_e32 v55, s31, v70
	v_med3_f32 v54, v54, s19, v135
	v_med3_f32 v55, v55, s19, v135
	v_cvt_pk_fp8_f32 v138, v54, v55
	s_waitcnt vmcnt(26)
	v_mul_f32_e32 v58, s31, v74
	v_med3_f32 v58, v58, s19, v135
	s_waitcnt vmcnt(25)
	v_mul_f32_e32 v59, s31, v90
	s_waitcnt vmcnt(23)
	v_mul_f32_e32 v65, s31, v102
	v_med3_f32 v54, v65, s19, v135
	s_waitcnt vmcnt(22)
	v_mul_f32_e32 v56, s31, v82
	s_waitcnt vmcnt(21)
	v_mul_f32_e32 v57, s31, v78
	v_cvt_pk_fp8_f32 v139, v58, v54
	v_med3_f32 v54, v56, s19, v135
	v_med3_f32 v55, v57, s19, v135
	v_cvt_pk_fp8_f32 v138, v54, v55 op_sel:[0,0,1]
	s_waitcnt vmcnt(20)
	v_mul_f32_e32 v54, s31, v94
	s_waitcnt vmcnt(19)
	v_mul_f32_e32 v55, s31, v98
	v_med3_f32 v54, v54, s19, v135
	v_med3_f32 v55, v55, s19, v135
	v_mul_f32_e32 v64, s31, v86
	v_cvt_pk_fp8_f32 v140, v54, v55
	v_med3_f32 v56, v59, s19, v135
	v_med3_f32 v57, v64, s19, v135
	v_cvt_pk_fp8_f32 v139, v56, v57 op_sel:[0,0,1]
	s_waitcnt vmcnt(18)
; __device__ __forceinline__ unsigned pk4_fp8(float a, float b, float c, float d) { int w = 0; w = __builtin_amdgcn_cvt_pk_fp8_f32(clamp448(a), clamp448(b), w, false); w = __builtin_amdgcn_cvt_pk_fp8_f32(clamp448(c), clamp448(d), w, true); return (unsigned)w; }
; __device__ __forceinline__ void transpose_item_f8(const float* W, int N, unsigned char* WT, int ldt, int kind, int off, int item, int lane, float scale) {
;     ...
;     for (int hh = 0; hh < 2; ++hh)
; #pragma unroll
;         for (int i = 0; i < 4; ++i) { v4u o; o.x = pg8::pk4_fp8(v[hh][0][i] * scale, v[hh][1][i] * scale, v[hh][2][i] * scale, v[hh][3][i] * scale); o.y = pg8::pk4_fp8(v[hh][4][i] * scale, v[hh][5][i] * scale, v[hh][6][i] * scale, v[hh][7][i] * scale);
;             o.z = pg8::pk4_fp8(v[hh][8][i] * scale, v[hh][9][i] * scale, v[hh][10][i] * scale, v[hh][11][i] * scale); o.w = pg8::pk4_fp8(v[hh][12][i] * scale, v[hh][13][i] * scale, v[hh][14][i] * scale, v[hh][15][i] * scale);
;             __builtin_nontemporal_store(o, (v4u*)(WT + (size_t)rowmap(kind, off, n + 32 * hh + i) * ldt + k0)); }
	v_mul_f32_e32 v56, s31, v114
	s_waitcnt vmcnt(17)
	v_mul_f32_e32 v54, s31, v106
	v_med3_f32 v55, v56, s19, v135
	v_med3_f32 v54, v54, s19, v135
	v_cvt_pk_fp8_f32 v140, v55, v54 op_sel:[0,0,1]
	s_waitcnt vmcnt(16)
	v_mul_f32_e32 v54, s31, v110
	s_waitcnt vmcnt(15)
	v_mul_f32_e32 v59, s31, v118
	v_med3_f32 v58, v54, s19, v135
	v_med3_f32 v59, v59, s19, v135
	v_cvt_pk_fp8_f32 v141, v58, v59
	s_waitcnt vmcnt(14)
	v_mul_f32_e32 v58, s31, v122
	s_waitcnt vmcnt(13)
	v_mul_f32_e32 v70, s31, v126
	v_med3_f32 v66, v58, s19, v135
	v_med3_f32 v70, v70, s19, v135
	v_cvt_pk_fp8_f32 v141, v66, v70 op_sel:[0,0,1]
	v_bitop3_b32 v66, s13, v136, v134 bitop3:0xc8
	v_or_b32_e32 v66, s2, v66
	v_add_u32_e32 v70, s30, v130
	v_cndmask_b32_e64 v66, v66, v70, s[4:5]
	v_ashrrev_i32_e32 v70, 31, v66
	global_load_dwordx4 v[54:57], v[60:61], off offset:128 nt
	v_mul_lo_u32 v70, s6, v70
	global_load_dwordx4 v[62:65], v[62:63], off offset:128 nt
	v_mul_lo_u32 v74, s7, v66
	global_load_dwordx4 v[58:61], v[142:143], off offset:128 nt
	v_mad_u64_u32 v[142:143], s[8:9], s6, v66, v[132:133]
	v_add3_u32 v143, v74, v143, v70
	v_mul_f32_e32 v66, s31, v67
	v_mul_f32_e32 v67, s31, v71
	global_store_dwordx4 v[142:143], v[138:141], off nt
	v_med3_f32 v66, v66, s19, v135
	v_med3_f32 v67, v67, s19, v135
	v_mov_b32_e32 v138, 0
	v_cvt_pk_fp8_f32 v138, v66, v67
	v_mul_f32_e32 v66, s31, v83
	v_mul_f32_e32 v67, s31, v79
	v_med3_f32 v66, v66, s19, v135
	v_med3_f32 v67, v67, s19, v135
	v_cvt_pk_fp8_f32 v138, v66, v67 op_sel:[0,0,1]
	v_mul_f32_e32 v66, s31, v75
	v_mul_f32_e32 v67, s31, v103
	v_med3_f32 v66, v66, s19, v135
	v_med3_f32 v67, v67, s19, v135
	v_mov_b32_e32 v139, 0
	v_cvt_pk_fp8_f32 v139, v66, v67
	v_mul_f32_e32 v66, s31, v91
	v_mul_f32_e32 v67, s31, v87
	v_med3_f32 v66, v66, s19, v135
	v_med3_f32 v67, v67, s19, v135
	v_cvt_pk_fp8_f32 v139, v66, v67 op_sel:[0,0,1]
	v_mul_f32_e32 v66, s31, v95
	v_mul_f32_e32 v67, s31, v99
	v_med3_f32 v66, v66, s19, v135
	v_med3_f32 v67, v67, s19, v135
	v_mov_b32_e32 v140, 0
	v_cvt_pk_fp8_f32 v140, v66, v67
	v_mul_f32_e32 v66, s31, v115
	v_mul_f32_e32 v67, s31, v107
	v_med3_f32 v66, v66, s19, v135
	v_med3_f32 v67, v67, s19, v135
	v_cvt_pk_fp8_f32 v140, v66, v67 op_sel:[0,0,1]
	v_mul_f32_e32 v66, s31, v111
	v_mul_f32_e32 v67, s31, v119
	v_med3_f32 v66, v66, s19, v135
	v_med3_f32 v67, v67, s19, v135
	v_mov_b32_e32 v141, 0
	v_cvt_pk_fp8_f32 v141, v66, v67
	v_mul_f32_e32 v66, s31, v123
	v_mul_f32_e32 v67, s31, v127
	v_med3_f32 v66, v66, s19, v135
	v_med3_f32 v67, v67, s19, v135
	v_cvt_pk_fp8_f32 v141, v66, v67 op_sel:[0,0,1]
	v_or_b32_e32 v66, 1, v130
	v_bitop3_b32 v67, v130, s20, 1 bitop3:0xc8
	v_add_u32_e32 v66, s30, v66
	v_or_b32_e32 v67, s2, v67
	v_cndmask_b32_e64 v66, v67, v66, s[4:5]
	v_ashrrev_i32_e32 v67, 31, v66
	v_mul_lo_u32 v70, s6, v67
	v_mul_lo_u32 v71, s7, v66
	v_mad_u64_u32 v[66:67], s[8:9], s6, v66, v[132:133]
	v_add3_u32 v67, v71, v67, v70
	global_store_dwordx4 v[66:67], v[138:141], off nt
	v_mul_f32_e32 v66, s31, v68
	v_mul_f32_e32 v67, s31, v72
	v_med3_f32 v66, v66, s19, v135
	v_med3_f32 v67, v67, s19, v135
	v_mov_b32_e32 v138, 0
	v_cvt_pk_fp8_f32 v138, v66, v67
	v_mul_f32_e32 v66, s31, v84
	v_mul_f32_e32 v67, s31, v80
	v_med3_f32 v66, v66, s19, v135
	v_med3_f32 v67, v67, s19, v135
	v_cvt_pk_fp8_f32 v138, v66, v67 op_sel:[0,0,1]
	v_mul_f32_e32 v66, s31, v76
	v_mul_f32_e32 v67, s31, v104
	v_med3_f32 v66, v66, s19, v135
	v_med3_f32 v67, v67, s19, v135
	v_mov_b32_e32 v139, 0
	v_cvt_pk_fp8_f32 v139, v66, v67
	v_mul_f32_e32 v66, s31, v92
	v_mul_f32_e32 v67, s31, v88
	v_med3_f32 v66, v66, s19, v135
	v_med3_f32 v67, v67, s19, v135
	v_cvt_pk_fp8_f32 v139, v66, v67 op_sel:[0,0,1]
	v_mul_f32_e32 v66, s31, v96
	v_mul_f32_e32 v67, s31, v100
	v_med3_f32 v66, v66, s19, v135
	v_med3_f32 v67, v67, s19, v135
	v_mov_b32_e32 v140, 0
	v_cvt_pk_fp8_f32 v140, v66, v67
	v_mul_f32_e32 v66, s31, v116
	v_mul_f32_e32 v67, s31, v108
	v_med3_f32 v66, v66, s19, v135
	v_med3_f32 v67, v67, s19, v135
	v_cvt_pk_fp8_f32 v140, v66, v67 op_sel:[0,0,1]
	v_mul_f32_e32 v66, s31, v112
	v_mul_f32_e32 v67, s31, v120
	v_med3_f32 v66, v66, s19, v135
	v_med3_f32 v67, v67, s19, v135
	v_mov_b32_e32 v141, 0
	v_cvt_pk_fp8_f32 v141, v66, v67
	v_mul_f32_e32 v66, s31, v124
	v_mul_f32_e32 v67, s31, v128
	v_med3_f32 v66, v66, s19, v135
	v_med3_f32 v67, v67, s19, v135
	v_cvt_pk_fp8_f32 v141, v66, v67 op_sel:[0,0,1]
	v_or_b32_e32 v66, 2, v130
	v_bitop3_b32 v67, v130, s21, 2 bitop3:0xc8
	v_add_u32_e32 v66, s30, v66
	v_or_b32_e32 v67, s2, v67
	v_cndmask_b32_e64 v66, v67, v66, s[4:5]
	v_ashrrev_i32_e32 v67, 31, v66
	v_mul_lo_u32 v68, s6, v67
	v_mul_lo_u32 v70, s7, v66
	v_mad_u64_u32 v[66:67], s[8:9], s6, v66, v[132:133]
	v_add3_u32 v67, v70, v67, v68
	global_store_dwordx4 v[66:67], v[138:141], off nt
	v_mul_f32_e32 v66, s31, v69
	v_mul_f32_e32 v67, s31, v73
	v_med3_f32 v69, v66, s19, v135
	v_med3_f32 v67, v67, s19, v135
	v_mov_b32_e32 v66, 0
	v_cvt_pk_fp8_f32 v66, v69, v67
	v_mul_f32_e32 v68, s31, v85
	v_mul_f32_e32 v67, s31, v81
	v_med3_f32 v68, v68, s19, v135
	v_med3_f32 v67, v67, s19, v135
	v_cvt_pk_fp8_f32 v66, v68, v67 op_sel:[0,0,1]
	v_mul_f32_e32 v67, s31, v77
	v_mul_f32_e32 v68, s31, v105
	v_med3_f32 v70, v67, s19, v135
	v_med3_f32 v68, v68, s19, v135
	v_mov_b32_e32 v67, 0
	v_cvt_pk_fp8_f32 v67, v70, v68
	v_mul_f32_e32 v69, s31, v93
	v_mul_f32_e32 v68, s31, v89
	v_med3_f32 v69, v69, s19, v135
	v_med3_f32 v68, v68, s19, v135
	v_cvt_pk_fp8_f32 v67, v69, v68 op_sel:[0,0,1]
	v_mul_f32_e32 v68, s31, v97
	v_mul_f32_e32 v69, s31, v101
	v_med3_f32 v71, v68, s19, v135
	v_med3_f32 v69, v69, s19, v135
	v_mov_b32_e32 v68, 0
	v_cvt_pk_fp8_f32 v68, v71, v69
	v_mul_f32_e32 v70, s31, v117
	v_mul_f32_e32 v69, s31, v109
	v_med3_f32 v70, v70, s19, v135
	v_med3_f32 v69, v69, s19, v135
	v_cvt_pk_fp8_f32 v68, v70, v69 op_sel:[0,0,1]
	v_mul_f32_e32 v69, s31, v113
	v_mul_f32_e32 v70, s31, v121
	v_med3_f32 v72, v69, s19, v135
	v_med3_f32 v70, v70, s19, v135
	v_mov_b32_e32 v69, 0
	v_cvt_pk_fp8_f32 v69, v72, v70
	v_mul_f32_e32 v71, s31, v125
	v_mul_f32_e32 v70, s31, v129
	v_med3_f32 v71, v71, s19, v135
	v_med3_f32 v70, v70, s19, v135
	v_cvt_pk_fp8_f32 v69, v71, v70 op_sel:[0,0,1]
	v_or_b32_e32 v70, 3, v130
	v_bitop3_b32 v71, v130, s22, 3 bitop3:0xc8
	v_add_u32_e32 v70, s30, v70
	v_or_b32_e32 v71, s2, v71
	v_cndmask_b32_e64 v72, v71, v70, s[4:5]
	v_ashrrev_i32_e32 v70, 31, v72
	v_mul_lo_u32 v73, s6, v70
	v_mad_u64_u32 v[70:71], s[8:9], s6, v72, v[132:133]
	v_mul_lo_u32 v72, s7, v72
	v_add3_u32 v71, v72, v71, v73
	s_waitcnt vmcnt(10)
; __device__ __forceinline__ unsigned pk4_fp8(float a, float b, float c, float d) { int w = 0; w = __builtin_amdgcn_cvt_pk_fp8_f32(clamp448(a), clamp448(b), w, false); w = __builtin_amdgcn_cvt_pk_fp8_f32(clamp448(c), clamp448(d), w, true); return (unsigned)w; }
; __device__ __forceinline__ void transpose_item_f8(const float* W, int N, unsigned char* WT, int ldt, int kind, int off, int item, int lane, float scale) {
;     ...
;     for (int hh = 0; hh < 2; ++hh)
; #pragma unroll
;         for (int i = 0; i < 4; ++i) { v4u o; o.x = pg8::pk4_fp8(v[hh][0][i] * scale, v[hh][1][i] * scale, v[hh][2][i] * scale, v[hh][3][i] * scale); o.y = pg8::pk4_fp8(v[hh][4][i] * scale, v[hh][5][i] * scale, v[hh][6][i] * scale, v[hh][7][i] * scale);
;             o.z = pg8::pk4_fp8(v[hh][8][i] * scale, v[hh][9][i] * scale, v[hh][10][i] * scale, v[hh][11][i] * scale); o.w = pg8::pk4_fp8(v[hh][12][i] * scale, v[hh][13][i] * scale, v[hh][14][i] * scale, v[hh][15][i] * scale);
;             __builtin_nontemporal_store(o, (v4u*)(WT + (size_t)rowmap(kind, off, n + 32 * hh + i) * ldt + k0)); }
	v_mul_f32_e32 v10, s31, v10
	s_waitcnt vmcnt(9)
	v_mul_f32_e32 v14, s31, v14
	global_store_dwordx4 v[70:71], v[66:69], off nt
	v_med3_f32 v10, v10, s19, v135
	v_med3_f32 v14, v14, s19, v135
	v_mov_b32_e32 v68, 0
	v_cvt_pk_fp8_f32 v68, v10, v14
	s_waitcnt vmcnt(9)
	v_mul_f32_e32 v18, s31, v18
	s_waitcnt vmcnt(8)
	v_mul_f32_e32 v6, s31, v6
	v_med3_f32 v10, v18, s19, v135
	v_med3_f32 v6, v6, s19, v135
	v_cvt_pk_fp8_f32 v68, v10, v6 op_sel:[0,0,1]
	s_waitcnt vmcnt(7)
	v_mul_f32_e32 v2, s31, v2
	s_waitcnt vmcnt(6)
	v_mul_f32_e32 v6, s31, v54
	v_med3_f32 v2, v2, s19, v135
	v_med3_f32 v6, v6, s19, v135
	v_mov_b32_e32 v69, 0
	v_mul_f32_e32 v42, s31, v42
	v_mul_f32_e32 v46, s31, v46
	v_mul_f32_e32 v30, s31, v30
	v_mul_f32_e32 v34, s31, v34
	v_cvt_pk_fp8_f32 v69, v2, v6
	v_med3_f32 v42, v42, s19, v135
	v_med3_f32 v46, v46, s19, v135
	v_mov_b32_e32 v66, 0
	v_med3_f32 v30, v30, s19, v135
	v_med3_f32 v34, v34, s19, v135
	v_mov_b32_e32 v67, 0
	v_cvt_pk_fp8_f32 v66, v42, v46
	v_cvt_pk_fp8_f32 v67, v30, v34
	s_waitcnt vmcnt(5)
	v_mul_f32_e32 v10, s31, v62
	s_waitcnt vmcnt(4)
	v_mul_f32_e32 v2, s31, v58
	v_med3_f32 v6, v10, s19, v135
	v_med3_f32 v2, v2, s19, v135
	v_or_b32_e32 v70, 32, v130
	v_mul_f32_e32 v50, s31, v50
	v_mul_f32_e32 v38, s31, v38
	v_mul_f32_e32 v26, s31, v26
	v_mul_f32_e32 v22, s31, v22
	v_cvt_pk_fp8_f32 v69, v6, v2 op_sel:[0,0,1]
	v_bitop3_b32 v6, v130, s23, 32 bitop3:0xc8
	v_med3_f32 v42, v50, s19, v135
	v_med3_f32 v38, v38, s19, v135
	v_med3_f32 v26, v26, s19, v135
	v_med3_f32 v22, v22, s19, v135
	v_add_u32_e32 v2, s30, v70
	v_or_b32_e32 v6, s2, v6
	v_cvt_pk_fp8_f32 v66, v42, v38 op_sel:[0,0,1]
	v_cvt_pk_fp8_f32 v67, v26, v22 op_sel:[0,0,1]
	v_cndmask_b32_e64 v2, v6, v2, s[4:5]
	v_ashrrev_i32_e32 v6, 31, v2
	v_mul_lo_u32 v6, s6, v6
	v_mad_u64_u32 v[70:71], s[8:9], s6, v2, v[132:133]
	v_mul_lo_u32 v2, s7, v2
	v_add3_u32 v71, v2, v71, v6
	v_mul_f32_e32 v2, s31, v43
	v_mul_f32_e32 v6, s31, v47
	global_store_dwordx4 v[70:71], v[66:69], off nt
	v_med3_f32 v2, v2, s19, v135
	v_med3_f32 v6, v6, s19, v135
	v_mov_b32_e32 v66, 0
	v_cvt_pk_fp8_f32 v66, v2, v6
	v_mul_f32_e32 v10, s31, v51
	v_mul_f32_e32 v2, s31, v39
	v_med3_f32 v6, v10, s19, v135
	v_med3_f32 v2, v2, s19, v135
	v_cvt_pk_fp8_f32 v66, v6, v2 op_sel:[0,0,1]
	v_mul_f32_e32 v2, s31, v31
	v_mul_f32_e32 v6, s31, v35
	v_med3_f32 v2, v2, s19, v135
	v_med3_f32 v6, v6, s19, v135
	v_mov_b32_e32 v67, 0
	v_cvt_pk_fp8_f32 v67, v2, v6
	v_mul_f32_e32 v10, s31, v27
	v_mul_f32_e32 v2, s31, v23
	v_med3_f32 v6, v10, s19, v135
	v_med3_f32 v2, v2, s19, v135
	v_cvt_pk_fp8_f32 v67, v6, v2 op_sel:[0,0,1]
	v_mul_f32_e32 v2, s31, v11
	v_mul_f32_e32 v6, s31, v15
	v_med3_f32 v2, v2, s19, v135
	v_med3_f32 v6, v6, s19, v135
	v_mov_b32_e32 v68, 0
	v_cvt_pk_fp8_f32 v68, v2, v6
	v_mul_f32_e32 v10, s31, v19
	v_mul_f32_e32 v2, s31, v7
	v_med3_f32 v6, v10, s19, v135
	v_med3_f32 v2, v2, s19, v135
	v_cvt_pk_fp8_f32 v68, v6, v2 op_sel:[0,0,1]
	v_mul_f32_e32 v2, s31, v3
	v_mul_f32_e32 v3, s31, v55
	v_med3_f32 v2, v2, s19, v135
	v_med3_f32 v3, v3, s19, v135
	v_mov_b32_e32 v69, 0
	v_cvt_pk_fp8_f32 v69, v2, v3
	v_mul_f32_e32 v6, s31, v63
	v_mul_f32_e32 v2, s31, v59
	v_med3_f32 v3, v6, s19, v135
	v_med3_f32 v2, v2, s19, v135
	v_cvt_pk_fp8_f32 v69, v3, v2 op_sel:[0,0,1]
	v_or_b32_e32 v2, 33, v130
	v_bitop3_b32 v3, v130, s26, 33 bitop3:0xc8
	v_add_u32_e32 v2, s30, v2
	v_or_b32_e32 v3, s2, v3
	v_cndmask_b32_e64 v6, v3, v2, s[4:5]
	v_ashrrev_i32_e32 v2, 31, v6
	v_mul_lo_u32 v7, s6, v2
	v_mad_u64_u32 v[2:3], s[8:9], s6, v6, v[132:133]
	v_mul_lo_u32 v6, s7, v6
	v_add3_u32 v3, v6, v3, v7
	global_store_dwordx4 v[2:3], v[66:69], off nt
	v_mul_f32_e32 v2, s31, v44
	v_mul_f32_e32 v3, s31, v48
	v_med3_f32 v2, v2, s19, v135
	v_med3_f32 v3, v3, s19, v135
	v_mov_b32_e32 v66, 0
	v_cvt_pk_fp8_f32 v66, v2, v3
	v_mul_f32_e32 v6, s31, v52
	v_mul_f32_e32 v2, s31, v40
	v_med3_f32 v3, v6, s19, v135
	v_med3_f32 v2, v2, s19, v135
	v_cvt_pk_fp8_f32 v66, v3, v2 op_sel:[0,0,1]
	v_mul_f32_e32 v2, s31, v32
	v_mul_f32_e32 v3, s31, v36
	v_med3_f32 v2, v2, s19, v135
	v_med3_f32 v3, v3, s19, v135
	v_mov_b32_e32 v67, 0
	v_cvt_pk_fp8_f32 v67, v2, v3
	v_mul_f32_e32 v6, s31, v28
	v_mul_f32_e32 v2, s31, v24
	v_med3_f32 v3, v6, s19, v135
	v_med3_f32 v2, v2, s19, v135
	v_cvt_pk_fp8_f32 v67, v3, v2 op_sel:[0,0,1]
	v_mul_f32_e32 v2, s31, v12
	v_mul_f32_e32 v3, s31, v16
	v_med3_f32 v2, v2, s19, v135
	v_med3_f32 v3, v3, s19, v135
	v_mov_b32_e32 v68, 0
	v_cvt_pk_fp8_f32 v68, v2, v3
	v_mul_f32_e32 v6, s31, v20
	v_mul_f32_e32 v2, s31, v8
	v_med3_f32 v3, v6, s19, v135
	v_med3_f32 v2, v2, s19, v135
	v_cvt_pk_fp8_f32 v68, v3, v2 op_sel:[0,0,1]
	v_mul_f32_e32 v2, s31, v4
	v_mul_f32_e32 v3, s31, v56
	v_med3_f32 v2, v2, s19, v135
	v_med3_f32 v3, v3, s19, v135
	v_mov_b32_e32 v69, 0
	v_cvt_pk_fp8_f32 v69, v2, v3
	v_mul_f32_e32 v4, s31, v64
	v_mul_f32_e32 v2, s31, v60
	v_med3_f32 v3, v4, s19, v135
	v_med3_f32 v2, v2, s19, v135
	v_cvt_pk_fp8_f32 v69, v3, v2 op_sel:[0,0,1]
	v_or_b32_e32 v2, 34, v130
	v_bitop3_b32 v3, v130, s27, 34 bitop3:0xc8
	v_add_u32_e32 v2, s30, v2
	v_or_b32_e32 v3, s2, v3
	v_cndmask_b32_e64 v4, v3, v2, s[4:5]
	v_ashrrev_i32_e32 v2, 31, v4
	v_mul_lo_u32 v6, s6, v2
	v_mad_u64_u32 v[2:3], s[8:9], s6, v4, v[132:133]
	v_mul_lo_u32 v4, s7, v4
	v_add3_u32 v3, v4, v3, v6
	global_store_dwordx4 v[2:3], v[66:69], off nt
	v_mul_f32_e32 v2, s31, v45
	v_mul_f32_e32 v3, s31, v49
	v_med3_f32 v6, v2, s19, v135
	v_med3_f32 v3, v3, s19, v135
	v_mov_b32_e32 v2, 0
	v_cvt_pk_fp8_f32 v2, v6, v3
	v_mul_f32_e32 v4, s31, v53
	v_mul_f32_e32 v3, s31, v41
	v_med3_f32 v4, v4, s19, v135
	v_med3_f32 v3, v3, s19, v135
	v_cvt_pk_fp8_f32 v2, v4, v3 op_sel:[0,0,1]
	v_mul_f32_e32 v3, s31, v33
	v_mul_f32_e32 v4, s31, v37
	v_med3_f32 v7, v3, s19, v135
	v_med3_f32 v4, v4, s19, v135
	v_mov_b32_e32 v3, 0
	v_cvt_pk_fp8_f32 v3, v7, v4
	v_mul_f32_e32 v6, s31, v29
	v_mul_f32_e32 v4, s31, v25
	v_med3_f32 v6, v6, s19, v135
	v_med3_f32 v4, v4, s19, v135
	v_cvt_pk_fp8_f32 v3, v6, v4 op_sel:[0,0,1]
	v_mul_f32_e32 v4, s31, v13
	v_mul_f32_e32 v6, s31, v17
	v_med3_f32 v8, v4, s19, v135
	v_med3_f32 v6, v6, s19, v135
	v_mov_b32_e32 v4, 0
	v_cvt_pk_fp8_f32 v4, v8, v6
	v_mul_f32_e32 v7, s31, v21
	v_mul_f32_e32 v6, s31, v9
	v_med3_f32 v7, v7, s19, v135
	v_med3_f32 v6, v6, s19, v135
	v_cvt_pk_fp8_f32 v4, v7, v6 op_sel:[0,0,1]
	v_mul_f32_e32 v5, s31, v5
	v_mul_f32_e32 v6, s31, v57
	v_med3_f32 v8, v5, s19, v135
	v_med3_f32 v6, v6, s19, v135
	v_mov_b32_e32 v5, 0
	v_cvt_pk_fp8_f32 v5, v8, v6
	v_mul_f32_e32 v7, s31, v65
	v_mul_f32_e32 v6, s31, v61
	v_med3_f32 v7, v7, s19, v135
	v_med3_f32 v6, v6, s19, v135
	v_cvt_pk_fp8_f32 v5, v7, v6 op_sel:[0,0,1]
	v_or_b32_e32 v6, 35, v130
	v_bitop3_b32 v7, v130, s28, 35 bitop3:0xc8
	v_add_u32_e32 v6, s30, v6
	v_or_b32_e32 v7, s2, v7
	v_cndmask_b32_e64 v8, v7, v6, s[4:5]
	v_ashrrev_i32_e32 v6, 31, v8
	v_mul_lo_u32 v9, s6, v6
	v_mad_u64_u32 v[6:7], s[4:5], s6, v8, v[132:133]
	v_mul_lo_u32 v8, s7, v8
	v_add3_u32 v7, v8, v7, v9
	global_store_dwordx4 v[6:7], v[2:5], off nt
	s_cbranch_scc0 .LBB0_246

; __device__ __forceinline__ void moe_convert(Frame& F, int lo, int hi, int rank, int nrank) {
;     ...
;     for (int it = lo + rank; it < hi; it += nrank) {
;         int r = it; const float* W; unsigned char* WT; int N, ldt, kind, off; float f8s;
;         if (r < 14336) { const int e = r / 1792; r -= e * 1792; W = F.in[IN_WMG] + (size_t)e * 2048 * DFFE; N = DFFE; WT = F.ws + WS_WGU1 + (size_t)e * 14336 * 2048; ldt = 2048; kind = 1; off = 0; f8s = 32.f; }
;         else if ((r -= 14336) < 14336) { const int e = r / 1792; r -= e * 1792; W = F.in[IN_WMU] + (size_t)e * 2048 * DFFE; N = DFFE; WT = F.ws + WS_WGU1 + (size_t)e * 14336 * 2048; ldt = 2048; kind = 1; off = 128; f8s = 256.f; }
;         else { r -= 14336; const int e = r / 1792; r -= e * 1792; W = F.in[IN_WMD] + (size_t)e * DFFE * 2048; N = 2048; WT = F.ws + WS_WDN1 + (size_t)e * 2048 * DFFE; ldt = DFFE; kind = 0; off = 0; f8s = 64.f; }
.Lsf0_notw0:
	s_cmp_gt_u32 s4, 7
	s_cbranch_scc1 .Lsf0_skip
	v_mov_b32_e32 v8, 0x20020
	ds_read_b32 v9, v8 offset:4
	v_mbcnt_lo_u32_b32 v2, -1, 0
	v_mbcnt_hi_u32_b32 v2, -1, v2
	s_waitcnt lgkmcnt(0)
	v_readfirstlane_b32 s5, v9
	s_cmp_ge_u32 s5, 112
	s_cbranch_scc1 .Lsf0_skip
	s_add_i32 s5, s4, -1
	s_lshl_b32 s5, s5, 14
	v_lshl_add_u32 v7, v2, 4, s5
	ds_write_b128 v7, v[160:163] offset:0
	ds_write_b128 v7, v[164:167] offset:1024
	ds_write_b128 v7, v[168:171] offset:2048
	ds_write_b128 v7, v[172:175] offset:3072
	ds_write_b128 v7, v[176:179] offset:4096
	ds_write_b128 v7, v[180:183] offset:5120
	ds_write_b128 v7, v[184:187] offset:6144
	ds_write_b128 v7, v[188:191] offset:7168
	ds_write_b128 v7, v[192:195] offset:8192
	ds_write_b128 v7, v[196:199] offset:9216
	ds_write_b128 v7, v[200:203] offset:10240
	ds_write_b128 v7, v[204:207] offset:11264
	ds_write_b128 v7, v[208:211] offset:12288
	ds_write_b128 v7, v[212:215] offset:13312
	ds_write_b128 v7, v[216:219] offset:14336
	ds_write_b128 v7, v[220:223] offset:15360
	v_readlane_b32 s6, v247, 0
	v_readlane_b32 s7, v247, 1
	s_load_dwordx2 s[10:11], s[6:7], 0xc0
	s_load_dwordx2 s[12:13], s[6:7], 0xc8
	v_readlane_b32 s33, v247, 6
	v_mov_b32_e32 v3, 0x43e00000
	v_cmp_eq_u32_e32 vcc, 0, v2
	s_mul_i32 s33, s33, 112
	s_nop 1
	v_cndmask_b32_e64 v18, 0, 1, vcc
	s_waitcnt lgkmcnt(0)
	s_mov_b32 s34, 1
.Lsf0_loop:
	ds_read_b32 v9, v8
	s_waitcnt lgkmcnt(0)
	v_readfirstlane_b32 s5, v9
	s_cmp_eq_u32 s5, 1
	s_cbranch_scc1 .Lsf0_done
	ds_add_rtn_u32 v9, v8, v18 offset:4
	s_waitcnt lgkmcnt(0)
	v_readfirstlane_b32 s18, v9
	s_cmp_ge_u32 s18, 112
	s_cbranch_scc1 .Lsf0_done
	s_add_i32 s18, s18, s33
	s_and_b32 s27, s18, 1
	s_lshr_b32 s19, s18, 1
	s_add_i32 s19, s19, 0x5000
	s_cmp_lt_u32 s19, 0x7000
	s_cbranch_scc0 .Lsf0_down
	s_add_i32 s20, s19, 0xffffc800
	s_lshr_b32 s21, s20, 8
	s_mul_i32 s21, s21, 37
	s_lshr_b32 s21, s21, 8
	s_mul_i32 s28, s21, 0x700
	s_sub_i32 s20, s20, s28
	s_mul_i32 s28, s21, 0x3800000
	s_add_u32 s14, s10, s28
	s_addc_u32 s15, s11, 0
	s_mul_i32 s28, s21, 0x1c00000
	s_add_u32 s28, s28, 0x7800000
	s_add_u32 s16, s86, s28
	s_addc_u32 s17, s87, 0
	s_movk_i32 s24, 0x7000
	s_movk_i32 s25, 0x800
	s_mov_b32 s26, 0x43800000
	s_lshr_b32 s22, s20, 4
	s_mul_i32 s22, s22, 0x2493
	s_lshr_b32 s22, s22, 16
	s_mul_i32 s28, s22, 0x70
	s_sub_i32 s23, s20, s28
	s_mov_b32 s29, 1
	s_branch .Lsf0_dec

; __device__ __forceinline__ void moe_convert(Frame& F, int lo, int hi, int rank, int nrank) {
;     ...
;     for (int it = lo + rank; it < hi; it += nrank) {
;         int r = it; const float* W; unsigned char* WT; int N, ldt, kind, off; float f8s;
;         if (r < 14336) { const int e = r / 1792; r -= e * 1792; W = F.in[IN_WMG] + (size_t)e * 2048 * DFFE; N = DFFE; WT = F.ws + WS_WGU1 + (size_t)e * 14336 * 2048; ldt = 2048; kind = 1; off = 0; f8s = 32.f; }
;         else if ((r -= 14336) < 14336) { const int e = r / 1792; r -= e * 1792; W = F.in[IN_WMU] + (size_t)e * 2048 * DFFE; N = DFFE; WT = F.ws + WS_WGU1 + (size_t)e * 14336 * 2048; ldt = 2048; kind = 1; off = 128; f8s = 256.f; }
;         else { r -= 14336; const int e = r / 1792; r -= e * 1792; W = F.in[IN_WMD] + (size_t)e * DFFE * 2048; N = 2048; WT = F.ws + WS_WDN1 + (size_t)e * 2048 * DFFE; ldt = DFFE; kind = 0; off = 0; f8s = 64.f; }
.Lsf1_loop:
	ds_read_b32 v9, v8
	s_waitcnt lgkmcnt(0)
	v_readfirstlane_b32 s5, v9
	s_cmp_eq_u32 s5, 2
	s_cbranch_scc1 .Lsf1_done
	ds_add_rtn_u32 v9, v8, v18 offset:4
	s_waitcnt lgkmcnt(0)
	v_readfirstlane_b32 s18, v9
	s_cmp_ge_u32 s18, 112
	s_cbranch_scc1 .Lsf1_done
	s_add_i32 s18, s18, s33
	s_and_b32 s27, s18, 1
	s_lshr_b32 s19, s18, 1
	s_add_i32 s19, s19, 0x5000
	s_cmp_lt_u32 s19, 0x7000
	s_cbranch_scc0 .Lsf1_down
	s_add_i32 s20, s19, 0xffffc800
	s_lshr_b32 s21, s20, 8
	s_mul_i32 s21, s21, 37
	s_lshr_b32 s21, s21, 8
	s_mul_i32 s28, s21, 0x700
	s_sub_i32 s20, s20, s28
	s_mul_i32 s28, s21, 0x3800000
	s_add_u32 s14, s10, s28
	s_addc_u32 s15, s11, 0
	s_mul_i32 s28, s21, 0x1c00000
	s_add_u32 s28, s28, 0x7800000
	s_add_u32 s16, s86, s28
	s_addc_u32 s17, s87, 0
	s_movk_i32 s24, 0x7000
	s_movk_i32 s25, 0x800
	s_mov_b32 s26, 0x43800000
	s_lshr_b32 s22, s20, 4
	s_mul_i32 s22, s22, 0x2493
	s_lshr_b32 s22, s22, 16
	s_mul_i32 s28, s22, 0x70
	s_sub_i32 s23, s20, s28
	s_mov_b32 s29, 1
	s_branch .Lsf1_dec

; __device__ __forceinline__ void moe_convert(Frame& F, int lo, int hi, int rank, int nrank) {
;     ...
;     for (int it = lo + rank; it < hi; it += nrank) {
;         int r = it; const float* W; unsigned char* WT; int N, ldt, kind, off; float f8s;
;         if (r < 14336) { const int e = r / 1792; r -= e * 1792; W = F.in[IN_WMG] + (size_t)e * 2048 * DFFE; N = DFFE; WT = F.ws + WS_WGU1 + (size_t)e * 14336 * 2048; ldt = 2048; kind = 1; off = 0; f8s = 32.f; }
;         else if ((r -= 14336) < 14336) { const int e = r / 1792; r -= e * 1792; W = F.in[IN_WMU] + (size_t)e * 2048 * DFFE; N = DFFE; WT = F.ws + WS_WGU1 + (size_t)e * 14336 * 2048; ldt = 2048; kind = 1; off = 128; f8s = 256.f; }
;         else { r -= 14336; const int e = r / 1792; r -= e * 1792; W = F.in[IN_WMD] + (size_t)e * DFFE * 2048; N = 2048; WT = F.ws + WS_WDN1 + (size_t)e * 2048 * DFFE; ldt = DFFE; kind = 0; off = 0; f8s = 64.f; }
.Lsf2_loop:
	ds_read_b32 v9, v8
	s_waitcnt lgkmcnt(0)
	v_readfirstlane_b32 s5, v9
	s_cmp_eq_u32 s5, 3
	s_cbranch_scc1 .Lsf2_done
	ds_add_rtn_u32 v9, v8, v18 offset:4
	s_waitcnt lgkmcnt(0)
	v_readfirstlane_b32 s18, v9
	s_cmp_ge_u32 s18, 112
	s_cbranch_scc1 .Lsf2_done
	s_add_i32 s18, s18, s33
	s_and_b32 s27, s18, 1
	s_lshr_b32 s19, s18, 1
	s_add_i32 s19, s19, 0x5000
	s_cmp_lt_u32 s19, 0x7000
	s_cbranch_scc0 .Lsf2_down
	s_add_i32 s20, s19, 0xffffc800
	s_lshr_b32 s21, s20, 8
	s_mul_i32 s21, s21, 37
	s_lshr_b32 s21, s21, 8
	s_mul_i32 s28, s21, 0x700
	s_sub_i32 s20, s20, s28
	s_mul_i32 s28, s21, 0x3800000
	s_add_u32 s14, s10, s28
	s_addc_u32 s15, s11, 0
	s_mul_i32 s28, s21, 0x1c00000
	s_add_u32 s28, s28, 0x7800000
	s_add_u32 s16, s86, s28
	s_addc_u32 s17, s87, 0
	s_movk_i32 s24, 0x7000
	s_movk_i32 s25, 0x800
	s_mov_b32 s26, 0x43800000
	s_lshr_b32 s22, s20, 4
	s_mul_i32 s22, s22, 0x2493
	s_lshr_b32 s22, s22, 16
	s_mul_i32 s28, s22, 0x70
	s_sub_i32 s23, s20, s28
	s_mov_b32 s29, 1
	s_branch .Lsf2_dec

; __device__ __forceinline__ void moe_convert(Frame& F, int lo, int hi, int rank, int nrank) {
;     ...
;     for (int it = lo + rank; it < hi; it += nrank) {
;         int r = it; const float* W; unsigned char* WT; int N, ldt, kind, off; float f8s;
;         if (r < 14336) { const int e = r / 1792; r -= e * 1792; W = F.in[IN_WMG] + (size_t)e * 2048 * DFFE; N = DFFE; WT = F.ws + WS_WGU1 + (size_t)e * 14336 * 2048; ldt = 2048; kind = 1; off = 0; f8s = 32.f; }
;         else if ((r -= 14336) < 14336) { const int e = r / 1792; r -= e * 1792; W = F.in[IN_WMU] + (size_t)e * 2048 * DFFE; N = DFFE; WT = F.ws + WS_WGU1 + (size_t)e * 14336 * 2048; ldt = 2048; kind = 1; off = 128; f8s = 256.f; }
;         else { r -= 14336; const int e = r / 1792; r -= e * 1792; W = F.in[IN_WMD] + (size_t)e * DFFE * 2048; N = 2048; WT = F.ws + WS_WDN1 + (size_t)e * 2048 * DFFE; ldt = DFFE; kind = 0; off = 0; f8s = 64.f; }
.Lsf3_loop:
	ds_read_b32 v9, v8
	s_waitcnt lgkmcnt(0)
	v_readfirstlane_b32 s5, v9
	s_cmp_eq_u32 s5, 4
	s_cbranch_scc1 .Lsf3_done
	ds_add_rtn_u32 v9, v8, v18 offset:4
	s_waitcnt lgkmcnt(0)
	v_readfirstlane_b32 s18, v9
	s_cmp_ge_u32 s18, 112
	s_cbranch_scc1 .Lsf3_done
	s_add_i32 s18, s18, s33
	s_and_b32 s27, s18, 1
	s_lshr_b32 s19, s18, 1
	s_add_i32 s19, s19, 0x5000
	s_cmp_lt_u32 s19, 0x7000
	s_cbranch_scc0 .Lsf3_down
	s_add_i32 s20, s19, 0xffffc800
	s_lshr_b32 s21, s20, 8
	s_mul_i32 s21, s21, 37
	s_lshr_b32 s21, s21, 8
	s_mul_i32 s28, s21, 0x700
	s_sub_i32 s20, s20, s28
	s_mul_i32 s28, s21, 0x3800000
	s_add_u32 s14, s10, s28
	s_addc_u32 s15, s11, 0
	s_mul_i32 s28, s21, 0x1c00000
	s_add_u32 s28, s28, 0x7800000
	s_add_u32 s16, s86, s28
	s_addc_u32 s17, s87, 0
	s_movk_i32 s24, 0x7000
	s_movk_i32 s25, 0x800
	s_mov_b32 s26, 0x43800000
	s_lshr_b32 s22, s20, 4
	s_mul_i32 s22, s22, 0x2493
	s_lshr_b32 s22, s22, 16
	s_mul_i32 s28, s22, 0x70
	s_sub_i32 s23, s20, s28
	s_mov_b32 s29, 1
	s_branch .Lsf3_dec

; __device__ __forceinline__ void moe_convert(Frame& F, int lo, int hi, int rank, int nrank) {
;     ...
;     for (int it = lo + rank; it < hi; it += nrank) {
;         int r = it; const float* W; unsigned char* WT; int N, ldt, kind, off; float f8s;
;         if (r < 14336) { const int e = r / 1792; r -= e * 1792; W = F.in[IN_WMG] + (size_t)e * 2048 * DFFE; N = DFFE; WT = F.ws + WS_WGU1 + (size_t)e * 14336 * 2048; ldt = 2048; kind = 1; off = 0; f8s = 32.f; }
;         else if ((r -= 14336) < 14336) { const int e = r / 1792; r -= e * 1792; W = F.in[IN_WMU] + (size_t)e * 2048 * DFFE; N = DFFE; WT = F.ws + WS_WGU1 + (size_t)e * 14336 * 2048; ldt = 2048; kind = 1; off = 128; f8s = 256.f; }
;         else { r -= 14336; const int e = r / 1792; r -= e * 1792; W = F.in[IN_WMD] + (size_t)e * DFFE * 2048; N = 2048; WT = F.ws + WS_WDN1 + (size_t)e * 2048 * DFFE; ldt = DFFE; kind = 0; off = 0; f8s = 64.f; }
.Lsf4_loop:
	ds_read_b32 v9, v8
	s_waitcnt lgkmcnt(0)
	v_readfirstlane_b32 s5, v9
	s_cmp_eq_u32 s5, 5
	s_cbranch_scc1 .Lsf4_done
	ds_add_rtn_u32 v9, v8, v18 offset:4
	s_waitcnt lgkmcnt(0)
	v_readfirstlane_b32 s18, v9
	s_cmp_ge_u32 s18, 112
	s_cbranch_scc1 .Lsf4_done
	s_add_i32 s18, s18, s33
	s_and_b32 s27, s18, 1
	s_lshr_b32 s19, s18, 1
	s_add_i32 s19, s19, 0x5000
	s_cmp_lt_u32 s19, 0x7000
	s_cbranch_scc0 .Lsf4_down
	s_add_i32 s20, s19, 0xffffc800
	s_lshr_b32 s21, s20, 8
	s_mul_i32 s21, s21, 37
	s_lshr_b32 s21, s21, 8
	s_mul_i32 s28, s21, 0x700
	s_sub_i32 s20, s20, s28
	s_mul_i32 s28, s21, 0x3800000
	s_add_u32 s14, s10, s28
	s_addc_u32 s15, s11, 0
	s_mul_i32 s28, s21, 0x1c00000
	s_add_u32 s28, s28, 0x7800000
	s_add_u32 s16, s86, s28
	s_addc_u32 s17, s87, 0
	s_movk_i32 s24, 0x7000
	s_movk_i32 s25, 0x800
	s_mov_b32 s26, 0x43800000
	s_lshr_b32 s22, s20, 4
	s_mul_i32 s22, s22, 0x2493
	s_lshr_b32 s22, s22, 16
	s_mul_i32 s28, s22, 0x70
	s_sub_i32 s23, s20, s28
	s_mov_b32 s29, 1
	s_branch .Lsf4_dec

; __device__ __forceinline__ void moe_convert(Frame& F, int lo, int hi, int rank, int nrank) {
;     ...
;     for (int it = lo + rank; it < hi; it += nrank) {
;         int r = it; const float* W; unsigned char* WT; int N, ldt, kind, off; float f8s;
;         if (r < 14336) { const int e = r / 1792; r -= e * 1792; W = F.in[IN_WMG] + (size_t)e * 2048 * DFFE; N = DFFE; WT = F.ws + WS_WGU1 + (size_t)e * 14336 * 2048; ldt = 2048; kind = 1; off = 0; f8s = 32.f; }
;         else if ((r -= 14336) < 14336) { const int e = r / 1792; r -= e * 1792; W = F.in[IN_WMU] + (size_t)e * 2048 * DFFE; N = DFFE; WT = F.ws + WS_WGU1 + (size_t)e * 14336 * 2048; ldt = 2048; kind = 1; off = 128; f8s = 256.f; }
;         else { r -= 14336; const int e = r / 1792; r -= e * 1792; W = F.in[IN_WMD] + (size_t)e * DFFE * 2048; N = 2048; WT = F.ws + WS_WDN1 + (size_t)e * 2048 * DFFE; ldt = DFFE; kind = 0; off = 0; f8s = 64.f; }
.Lsf5_loop:
	ds_read_b32 v9, v8
	s_waitcnt lgkmcnt(0)
	v_readfirstlane_b32 s5, v9
	s_cmp_eq_u32 s5, 6
	s_cbranch_scc1 .Lsf5_done
	ds_add_rtn_u32 v9, v8, v18 offset:4
	s_waitcnt lgkmcnt(0)
	v_readfirstlane_b32 s18, v9
	s_cmp_ge_u32 s18, 112
	s_cbranch_scc1 .Lsf5_done
	s_add_i32 s18, s18, s33
	s_and_b32 s27, s18, 1
	s_lshr_b32 s19, s18, 1
	s_add_i32 s19, s19, 0x5000
	s_cmp_lt_u32 s19, 0x7000
	s_cbranch_scc0 .Lsf5_down
	s_add_i32 s20, s19, 0xffffc800
	s_lshr_b32 s21, s20, 8
	s_mul_i32 s21, s21, 37
	s_lshr_b32 s21, s21, 8
	s_mul_i32 s28, s21, 0x700
	s_sub_i32 s20, s20, s28
	s_mul_i32 s28, s21, 0x3800000
	s_add_u32 s14, s10, s28
	s_addc_u32 s15, s11, 0
	s_mul_i32 s28, s21, 0x1c00000
	s_add_u32 s28, s28, 0x7800000
	s_add_u32 s16, s86, s28
	s_addc_u32 s17, s87, 0
	s_movk_i32 s24, 0x7000
	s_movk_i32 s25, 0x800
	s_mov_b32 s26, 0x43800000
	s_lshr_b32 s22, s20, 4
	s_mul_i32 s22, s22, 0x2493
	s_lshr_b32 s22, s22, 16
	s_mul_i32 s28, s22, 0x70
	s_sub_i32 s23, s20, s28
	s_mov_b32 s29, 1
	s_branch .Lsf5_dec

; __device__ __forceinline__ void moe_convert(Frame& F, int lo, int hi, int rank, int nrank) {
;     ...
;     for (int it = lo + rank; it < hi; it += nrank) {
;         int r = it; const float* W; unsigned char* WT; int N, ldt, kind, off; float f8s;
;         if (r < 14336) { const int e = r / 1792; r -= e * 1792; W = F.in[IN_WMG] + (size_t)e * 2048 * DFFE; N = DFFE; WT = F.ws + WS_WGU1 + (size_t)e * 14336 * 2048; ldt = 2048; kind = 1; off = 0; f8s = 32.f; }
;         else if ((r -= 14336) < 14336) { const int e = r / 1792; r -= e * 1792; W = F.in[IN_WMU] + (size_t)e * 2048 * DFFE; N = DFFE; WT = F.ws + WS_WGU1 + (size_t)e * 14336 * 2048; ldt = 2048; kind = 1; off = 128; f8s = 256.f; }
;         else { r -= 14336; const int e = r / 1792; r -= e * 1792; W = F.in[IN_WMD] + (size_t)e * DFFE * 2048; N = 2048; WT = F.ws + WS_WDN1 + (size_t)e * 2048 * DFFE; ldt = DFFE; kind = 0; off = 0; f8s = 64.f; }
.Lsf6_loop:
	ds_read_b32 v9, v8
	s_waitcnt lgkmcnt(0)
	v_readfirstlane_b32 s5, v9
	s_cmp_eq_u32 s5, 7
	s_cbranch_scc1 .Lsf6_done
	ds_add_rtn_u32 v9, v8, v18 offset:4
	s_waitcnt lgkmcnt(0)
	v_readfirstlane_b32 s18, v9
	s_cmp_ge_u32 s18, 112
	s_cbranch_scc1 .Lsf6_done
	s_add_i32 s18, s18, s33
	s_and_b32 s27, s18, 1
	s_lshr_b32 s19, s18, 1
	s_add_i32 s19, s19, 0x5000
	s_cmp_lt_u32 s19, 0x7000
	s_cbranch_scc0 .Lsf6_down
	s_add_i32 s20, s19, 0xffffc800
	s_lshr_b32 s21, s20, 8
	s_mul_i32 s21, s21, 37
	s_lshr_b32 s21, s21, 8
	s_mul_i32 s28, s21, 0x700
	s_sub_i32 s20, s20, s28
	s_mul_i32 s28, s21, 0x3800000
	s_add_u32 s14, s10, s28
	s_addc_u32 s15, s11, 0
	s_mul_i32 s28, s21, 0x1c00000
	s_add_u32 s28, s28, 0x7800000
	s_add_u32 s16, s86, s28
	s_addc_u32 s17, s87, 0
	s_movk_i32 s24, 0x7000
	s_movk_i32 s25, 0x800
	s_mov_b32 s26, 0x43800000
	s_lshr_b32 s22, s20, 4
	s_mul_i32 s22, s22, 0x2493
	s_lshr_b32 s22, s22, 16
	s_mul_i32 s28, s22, 0x70
	s_sub_i32 s23, s20, s28
	s_mov_b32 s29, 1
	s_branch .Lsf6_dec

; __device__ __forceinline__ void moe_convert(Frame& F, int lo, int hi, int rank, int nrank) {
;     ...
;     for (int it = lo + rank; it < hi; it += nrank) {
;         int r = it; const float* W; unsigned char* WT; int N, ldt, kind, off; float f8s;
;         if (r < 14336) { const int e = r / 1792; r -= e * 1792; W = F.in[IN_WMG] + (size_t)e * 2048 * DFFE; N = DFFE; WT = F.ws + WS_WGU1 + (size_t)e * 14336 * 2048; ldt = 2048; kind = 1; off = 0; f8s = 32.f; }
;         else if ((r -= 14336) < 14336) { const int e = r / 1792; r -= e * 1792; W = F.in[IN_WMU] + (size_t)e * 2048 * DFFE; N = DFFE; WT = F.ws + WS_WGU1 + (size_t)e * 14336 * 2048; ldt = 2048; kind = 1; off = 128; f8s = 256.f; }
;         else { r -= 14336; const int e = r / 1792; r -= e * 1792; W = F.in[IN_WMD] + (size_t)e * DFFE * 2048; N = 2048; WT = F.ws + WS_WDN1 + (size_t)e * 2048 * DFFE; ldt = DFFE; kind = 0; off = 0; f8s = 64.f; }
.Lsf7_loop:
	ds_read_b32 v9, v8
	s_waitcnt lgkmcnt(0)
	v_readfirstlane_b32 s5, v9
	s_cmp_eq_u32 s5, 8
	s_cbranch_scc1 .Lsf7_done
	ds_add_rtn_u32 v9, v8, v18 offset:4
	s_waitcnt lgkmcnt(0)
	v_readfirstlane_b32 s18, v9
	s_cmp_ge_u32 s18, 112
	s_cbranch_scc1 .Lsf7_done
	s_add_i32 s18, s18, s33
	s_and_b32 s27, s18, 1
	s_lshr_b32 s19, s18, 1
	s_add_i32 s19, s19, 0x5000
	s_cmp_lt_u32 s19, 0x7000
	s_cbranch_scc0 .Lsf7_down
	s_add_i32 s20, s19, 0xffffc800
	s_lshr_b32 s21, s20, 8
	s_mul_i32 s21, s21, 37
	s_lshr_b32 s21, s21, 8
	s_mul_i32 s28, s21, 0x700
	s_sub_i32 s20, s20, s28
	s_mul_i32 s28, s21, 0x3800000
	s_add_u32 s14, s10, s28
	s_addc_u32 s15, s11, 0
	s_mul_i32 s28, s21, 0x1c00000
	s_add_u32 s28, s28, 0x7800000
	s_add_u32 s16, s86, s28
	s_addc_u32 s17, s87, 0
	s_movk_i32 s24, 0x7000
	s_movk_i32 s25, 0x800
	s_mov_b32 s26, 0x43800000
	s_lshr_b32 s22, s20, 4
	s_mul_i32 s22, s22, 0x2493
	s_lshr_b32 s22, s22, 16
	s_mul_i32 s28, s22, 0x70
	s_sub_i32 s23, s20, s28
	s_mov_b32 s29, 1
	s_branch .Lsf7_dec

; __device__ __forceinline__ void moe_convert(Frame& F, int lo, int hi, int rank, int nrank) {
;     ...
;     for (int it = lo + rank; it < hi; it += nrank) {
;         int r = it; const float* W; unsigned char* WT; int N, ldt, kind, off; float f8s;
;         if (r < 14336) { const int e = r / 1792; r -= e * 1792; W = F.in[IN_WMG] + (size_t)e * 2048 * DFFE; N = DFFE; WT = F.ws + WS_WGU1 + (size_t)e * 14336 * 2048; ldt = 2048; kind = 1; off = 0; f8s = 32.f; }
;         else if ((r -= 14336) < 14336) { const int e = r / 1792; r -= e * 1792; W = F.in[IN_WMU] + (size_t)e * 2048 * DFFE; N = DFFE; WT = F.ws + WS_WGU1 + (size_t)e * 14336 * 2048; ldt = 2048; kind = 1; off = 128; f8s = 256.f; }
;         else { r -= 14336; const int e = r / 1792; r -= e * 1792; W = F.in[IN_WMD] + (size_t)e * DFFE * 2048; N = 2048; WT = F.ws + WS_WDN1 + (size_t)e * 2048 * DFFE; ldt = DFFE; kind = 0; off = 0; f8s = 64.f; }
.Lsf8_loop:
	ds_read_b32 v9, v8
	s_waitcnt lgkmcnt(0)
	v_readfirstlane_b32 s5, v9
	s_cmp_eq_u32 s5, 9
	s_cbranch_scc1 .Lsf8_done
	ds_add_rtn_u32 v9, v8, v18 offset:4
	s_waitcnt lgkmcnt(0)
	v_readfirstlane_b32 s18, v9
	s_cmp_ge_u32 s18, 112
	s_cbranch_scc1 .Lsf8_done
	s_add_i32 s18, s18, s33
	s_and_b32 s27, s18, 1
	s_lshr_b32 s19, s18, 1
	s_add_i32 s19, s19, 0x5000
	s_cmp_lt_u32 s19, 0x7000
	s_cbranch_scc0 .Lsf8_down
	s_add_i32 s20, s19, 0xffffc800
	s_lshr_b32 s21, s20, 8
	s_mul_i32 s21, s21, 37
	s_lshr_b32 s21, s21, 8
	s_mul_i32 s28, s21, 0x700
	s_sub_i32 s20, s20, s28
	s_mul_i32 s28, s21, 0x3800000
	s_add_u32 s14, s10, s28
	s_addc_u32 s15, s11, 0
	s_mul_i32 s28, s21, 0x1c00000
	s_add_u32 s28, s28, 0x7800000
	s_add_u32 s16, s86, s28
	s_addc_u32 s17, s87, 0
	s_movk_i32 s24, 0x7000
	s_movk_i32 s25, 0x800
	s_mov_b32 s26, 0x43800000
	s_lshr_b32 s22, s20, 4
	s_mul_i32 s22, s22, 0x2493
	s_lshr_b32 s22, s22, 16
	s_mul_i32 s28, s22, 0x70
	s_sub_i32 s23, s20, s28
	s_mov_b32 s29, 1
	s_branch .Lsf8_dec

; __device__ __forceinline__ void moe_convert(Frame& F, int lo, int hi, int rank, int nrank) {
;     ...
;     for (int it = lo + rank; it < hi; it += nrank) {
;         int r = it; const float* W; unsigned char* WT; int N, ldt, kind, off; float f8s;
;         if (r < 14336) { const int e = r / 1792; r -= e * 1792; W = F.in[IN_WMG] + (size_t)e * 2048 * DFFE; N = DFFE; WT = F.ws + WS_WGU1 + (size_t)e * 14336 * 2048; ldt = 2048; kind = 1; off = 0; f8s = 32.f; }
;         else if ((r -= 14336) < 14336) { const int e = r / 1792; r -= e * 1792; W = F.in[IN_WMU] + (size_t)e * 2048 * DFFE; N = DFFE; WT = F.ws + WS_WGU1 + (size_t)e * 14336 * 2048; ldt = 2048; kind = 1; off = 128; f8s = 256.f; }
;         else { r -= 14336; const int e = r / 1792; r -= e * 1792; W = F.in[IN_WMD] + (size_t)e * DFFE * 2048; N = 2048; WT = F.ws + WS_WDN1 + (size_t)e * 2048 * DFFE; ldt = DFFE; kind = 0; off = 0; f8s = 64.f; }
.Lsf9_loop:
	ds_read_b32 v9, v8
	s_waitcnt lgkmcnt(0)
	v_readfirstlane_b32 s5, v9
	s_cmp_eq_u32 s5, 10
	s_cbranch_scc1 .Lsf9_done
	ds_add_rtn_u32 v9, v8, v18 offset:4
	s_waitcnt lgkmcnt(0)
	v_readfirstlane_b32 s18, v9
	s_cmp_ge_u32 s18, 112
	s_cbranch_scc1 .Lsf9_done
	s_add_i32 s18, s18, s33
	s_and_b32 s27, s18, 1
	s_lshr_b32 s19, s18, 1
	s_add_i32 s19, s19, 0x5000
	s_cmp_lt_u32 s19, 0x7000
	s_cbranch_scc0 .Lsf9_down
	s_add_i32 s20, s19, 0xffffc800
	s_lshr_b32 s21, s20, 8
	s_mul_i32 s21, s21, 37
	s_lshr_b32 s21, s21, 8
	s_mul_i32 s28, s21, 0x700
	s_sub_i32 s20, s20, s28
	s_mul_i32 s28, s21, 0x3800000
	s_add_u32 s14, s10, s28
	s_addc_u32 s15, s11, 0
	s_mul_i32 s28, s21, 0x1c00000
	s_add_u32 s28, s28, 0x7800000
	s_add_u32 s16, s86, s28
	s_addc_u32 s17, s87, 0
	s_movk_i32 s24, 0x7000
	s_movk_i32 s25, 0x800
	s_mov_b32 s26, 0x43800000
	s_lshr_b32 s22, s20, 4
	s_mul_i32 s22, s22, 0x2493
	s_lshr_b32 s22, s22, 16
	s_mul_i32 s28, s22, 0x70
	s_sub_i32 s23, s20, s28
	s_mov_b32 s29, 1
	s_branch .Lsf9_dec

; __device__ __forceinline__ void moe_convert(Frame& F, int lo, int hi, int rank, int nrank) {
;     ...
;     for (int it = lo + rank; it < hi; it += nrank) {
;         int r = it; const float* W; unsigned char* WT; int N, ldt, kind, off; float f8s;
;         if (r < 14336) { const int e = r / 1792; r -= e * 1792; W = F.in[IN_WMG] + (size_t)e * 2048 * DFFE; N = DFFE; WT = F.ws + WS_WGU1 + (size_t)e * 14336 * 2048; ldt = 2048; kind = 1; off = 0; f8s = 32.f; }
;         else if ((r -= 14336) < 14336) { const int e = r / 1792; r -= e * 1792; W = F.in[IN_WMU] + (size_t)e * 2048 * DFFE; N = DFFE; WT = F.ws + WS_WGU1 + (size_t)e * 14336 * 2048; ldt = 2048; kind = 1; off = 128; f8s = 256.f; }
;         else { r -= 14336; const int e = r / 1792; r -= e * 1792; W = F.in[IN_WMD] + (size_t)e * DFFE * 2048; N = 2048; WT = F.ws + WS_WDN1 + (size_t)e * 2048 * DFFE; ldt = DFFE; kind = 0; off = 0; f8s = 64.f; }
.Lsf10_loop:
	ds_read_b32 v9, v8
	s_waitcnt lgkmcnt(0)
	v_readfirstlane_b32 s5, v9
	s_cmp_eq_u32 s5, 11
	s_cbranch_scc1 .Lsf10_done
	ds_add_rtn_u32 v9, v8, v18 offset:4
	s_waitcnt lgkmcnt(0)
	v_readfirstlane_b32 s18, v9
	s_cmp_ge_u32 s18, 112
	s_cbranch_scc1 .Lsf10_done
	s_add_i32 s18, s18, s33
	s_and_b32 s27, s18, 1
	s_lshr_b32 s19, s18, 1
	s_add_i32 s19, s19, 0x5000
	s_cmp_lt_u32 s19, 0x7000
	s_cbranch_scc0 .Lsf10_down
	s_add_i32 s20, s19, 0xffffc800
	s_lshr_b32 s21, s20, 8
	s_mul_i32 s21, s21, 37
	s_lshr_b32 s21, s21, 8
	s_mul_i32 s28, s21, 0x700
	s_sub_i32 s20, s20, s28
	s_mul_i32 s28, s21, 0x3800000
	s_add_u32 s14, s10, s28
	s_addc_u32 s15, s11, 0
	s_mul_i32 s28, s21, 0x1c00000
	s_add_u32 s28, s28, 0x7800000
	s_add_u32 s16, s86, s28
	s_addc_u32 s17, s87, 0
	s_movk_i32 s24, 0x7000
	s_movk_i32 s25, 0x800
	s_mov_b32 s26, 0x43800000
	s_lshr_b32 s22, s20, 4
	s_mul_i32 s22, s22, 0x2493
	s_lshr_b32 s22, s22, 16
	s_mul_i32 s28, s22, 0x70
	s_sub_i32 s23, s20, s28
	s_mov_b32 s29, 1
	s_branch .Lsf10_dec

; __device__ __forceinline__ void moe_convert(Frame& F, int lo, int hi, int rank, int nrank) {
;     ...
;     for (int it = lo + rank; it < hi; it += nrank) {
;         int r = it; const float* W; unsigned char* WT; int N, ldt, kind, off; float f8s;
;         if (r < 14336) { const int e = r / 1792; r -= e * 1792; W = F.in[IN_WMG] + (size_t)e * 2048 * DFFE; N = DFFE; WT = F.ws + WS_WGU1 + (size_t)e * 14336 * 2048; ldt = 2048; kind = 1; off = 0; f8s = 32.f; }
;         else if ((r -= 14336) < 14336) { const int e = r / 1792; r -= e * 1792; W = F.in[IN_WMU] + (size_t)e * 2048 * DFFE; N = DFFE; WT = F.ws + WS_WGU1 + (size_t)e * 14336 * 2048; ldt = 2048; kind = 1; off = 128; f8s = 256.f; }
;         else { r -= 14336; const int e = r / 1792; r -= e * 1792; W = F.in[IN_WMD] + (size_t)e * DFFE * 2048; N = 2048; WT = F.ws + WS_WDN1 + (size_t)e * 2048 * DFFE; ldt = DFFE; kind = 0; off = 0; f8s = 64.f; }
.Lsf11_loop:
	ds_read_b32 v9, v8
	s_waitcnt lgkmcnt(0)
	v_readfirstlane_b32 s5, v9
	s_cmp_eq_u32 s5, 12
	s_cbranch_scc1 .Lsf11_done
	ds_add_rtn_u32 v9, v8, v18 offset:4
	s_waitcnt lgkmcnt(0)
	v_readfirstlane_b32 s18, v9
	s_cmp_ge_u32 s18, 112
	s_cbranch_scc1 .Lsf11_done
	s_add_i32 s18, s18, s33
	s_and_b32 s27, s18, 1
	s_lshr_b32 s19, s18, 1
	s_add_i32 s19, s19, 0x5000
	s_cmp_lt_u32 s19, 0x7000
	s_cbranch_scc0 .Lsf11_down
	s_add_i32 s20, s19, 0xffffc800
	s_lshr_b32 s21, s20, 8
	s_mul_i32 s21, s21, 37
	s_lshr_b32 s21, s21, 8
	s_mul_i32 s28, s21, 0x700
	s_sub_i32 s20, s20, s28
	s_mul_i32 s28, s21, 0x3800000
	s_add_u32 s14, s10, s28
	s_addc_u32 s15, s11, 0
	s_mul_i32 s28, s21, 0x1c00000
	s_add_u32 s28, s28, 0x7800000
	s_add_u32 s16, s86, s28
	s_addc_u32 s17, s87, 0
	s_movk_i32 s24, 0x7000
	s_movk_i32 s25, 0x800
	s_mov_b32 s26, 0x43800000
	s_lshr_b32 s22, s20, 4
	s_mul_i32 s22, s22, 0x2493
	s_lshr_b32 s22, s22, 16
	s_mul_i32 s28, s22, 0x70
	s_sub_i32 s23, s20, s28
	s_mov_b32 s29, 1
	s_branch .Lsf11_dec

; __device__ __forceinline__ void moe_convert(Frame& F, int lo, int hi, int rank, int nrank) {
;     ...
;     for (int it = lo + rank; it < hi; it += nrank) {
;         int r = it; const float* W; unsigned char* WT; int N, ldt, kind, off; float f8s;
;         if (r < 14336) { const int e = r / 1792; r -= e * 1792; W = F.in[IN_WMG] + (size_t)e * 2048 * DFFE; N = DFFE; WT = F.ws + WS_WGU1 + (size_t)e * 14336 * 2048; ldt = 2048; kind = 1; off = 0; f8s = 32.f; }
;         else if ((r -= 14336) < 14336) { const int e = r / 1792; r -= e * 1792; W = F.in[IN_WMU] + (size_t)e * 2048 * DFFE; N = DFFE; WT = F.ws + WS_WGU1 + (size_t)e * 14336 * 2048; ldt = 2048; kind = 1; off = 128; f8s = 256.f; }
;         else { r -= 14336; const int e = r / 1792; r -= e * 1792; W = F.in[IN_WMD] + (size_t)e * DFFE * 2048; N = 2048; WT = F.ws + WS_WDN1 + (size_t)e * 2048 * DFFE; ldt = DFFE; kind = 0; off = 0; f8s = 64.f; }
.Lsf12_loop:
	ds_read_b32 v9, v8
	s_waitcnt lgkmcnt(0)
	v_readfirstlane_b32 s5, v9
	s_cmp_eq_u32 s5, 13
	s_cbranch_scc1 .Lsf12_done
	ds_add_rtn_u32 v9, v8, v18 offset:4
	s_waitcnt lgkmcnt(0)
	v_readfirstlane_b32 s18, v9
	s_cmp_ge_u32 s18, 112
	s_cbranch_scc1 .Lsf12_done
	s_add_i32 s18, s18, s33
	s_and_b32 s27, s18, 1
	s_lshr_b32 s19, s18, 1
	s_add_i32 s19, s19, 0x5000
	s_cmp_lt_u32 s19, 0x7000
	s_cbranch_scc0 .Lsf12_down
	s_add_i32 s20, s19, 0xffffc800
	s_lshr_b32 s21, s20, 8
	s_mul_i32 s21, s21, 37
	s_lshr_b32 s21, s21, 8
	s_mul_i32 s28, s21, 0x700
	s_sub_i32 s20, s20, s28
	s_mul_i32 s28, s21, 0x3800000
	s_add_u32 s14, s10, s28
	s_addc_u32 s15, s11, 0
	s_mul_i32 s28, s21, 0x1c00000
	s_add_u32 s28, s28, 0x7800000
	s_add_u32 s16, s86, s28
	s_addc_u32 s17, s87, 0
	s_movk_i32 s24, 0x7000
	s_movk_i32 s25, 0x800
	s_mov_b32 s26, 0x43800000
	s_lshr_b32 s22, s20, 4
	s_mul_i32 s22, s22, 0x2493
	s_lshr_b32 s22, s22, 16
	s_mul_i32 s28, s22, 0x70
	s_sub_i32 s23, s20, s28
	s_mov_b32 s29, 1
	s_branch .Lsf12_dec

; __device__ __forceinline__ void moe_convert(Frame& F, int lo, int hi, int rank, int nrank) {
;     ...
;     for (int it = lo + rank; it < hi; it += nrank) {
;         int r = it; const float* W; unsigned char* WT; int N, ldt, kind, off; float f8s;
;         if (r < 14336) { const int e = r / 1792; r -= e * 1792; W = F.in[IN_WMG] + (size_t)e * 2048 * DFFE; N = DFFE; WT = F.ws + WS_WGU1 + (size_t)e * 14336 * 2048; ldt = 2048; kind = 1; off = 0; f8s = 32.f; }
;         else if ((r -= 14336) < 14336) { const int e = r / 1792; r -= e * 1792; W = F.in[IN_WMU] + (size_t)e * 2048 * DFFE; N = DFFE; WT = F.ws + WS_WGU1 + (size_t)e * 14336 * 2048; ldt = 2048; kind = 1; off = 128; f8s = 256.f; }
;         else { r -= 14336; const int e = r / 1792; r -= e * 1792; W = F.in[IN_WMD] + (size_t)e * DFFE * 2048; N = 2048; WT = F.ws + WS_WDN1 + (size_t)e * 2048 * DFFE; ldt = DFFE; kind = 0; off = 0; f8s = 64.f; }
.Lsf13_loop:
	ds_read_b32 v9, v8
	s_waitcnt lgkmcnt(0)
	v_readfirstlane_b32 s5, v9
	s_cmp_eq_u32 s5, 14
	s_cbranch_scc1 .Lsf13_done
	ds_add_rtn_u32 v9, v8, v18 offset:4
	s_waitcnt lgkmcnt(0)
	v_readfirstlane_b32 s18, v9
	s_cmp_ge_u32 s18, 112
	s_cbranch_scc1 .Lsf13_done
	s_add_i32 s18, s18, s33
	s_and_b32 s27, s18, 1
	s_lshr_b32 s19, s18, 1
	s_add_i32 s19, s19, 0x5000
	s_cmp_lt_u32 s19, 0x7000
	s_cbranch_scc0 .Lsf13_down
	s_add_i32 s20, s19, 0xffffc800
	s_lshr_b32 s21, s20, 8
	s_mul_i32 s21, s21, 37
	s_lshr_b32 s21, s21, 8
	s_mul_i32 s28, s21, 0x700
	s_sub_i32 s20, s20, s28
	s_mul_i32 s28, s21, 0x3800000
	s_add_u32 s14, s10, s28
	s_addc_u32 s15, s11, 0
	s_mul_i32 s28, s21, 0x1c00000
	s_add_u32 s28, s28, 0x7800000
	s_add_u32 s16, s86, s28
	s_addc_u32 s17, s87, 0
	s_movk_i32 s24, 0x7000
	s_movk_i32 s25, 0x800
	s_mov_b32 s26, 0x43800000
	s_lshr_b32 s22, s20, 4
	s_mul_i32 s22, s22, 0x2493
	s_lshr_b32 s22, s22, 16
	s_mul_i32 s28, s22, 0x70
	s_sub_i32 s23, s20, s28
	s_mov_b32 s29, 1
	s_branch .Lsf13_dec

; __device__ __forceinline__ void moe_convert(Frame& F, int lo, int hi, int rank, int nrank) {
;     ...
;     for (int it = lo + rank; it < hi; it += nrank) {
;         int r = it; const float* W; unsigned char* WT; int N, ldt, kind, off; float f8s;
;         if (r < 14336) { const int e = r / 1792; r -= e * 1792; W = F.in[IN_WMG] + (size_t)e * 2048 * DFFE; N = DFFE; WT = F.ws + WS_WGU1 + (size_t)e * 14336 * 2048; ldt = 2048; kind = 1; off = 0; f8s = 32.f; }
;         else if ((r -= 14336) < 14336) { const int e = r / 1792; r -= e * 1792; W = F.in[IN_WMU] + (size_t)e * 2048 * DFFE; N = DFFE; WT = F.ws + WS_WGU1 + (size_t)e * 14336 * 2048; ldt = 2048; kind = 1; off = 128; f8s = 256.f; }
;         else { r -= 14336; const int e = r / 1792; r -= e * 1792; W = F.in[IN_WMD] + (size_t)e * DFFE * 2048; N = 2048; WT = F.ws + WS_WDN1 + (size_t)e * 2048 * DFFE; ldt = DFFE; kind = 0; off = 0; f8s = 64.f; }
.Lsf14_notw0:
	s_cmp_gt_u32 s4, 7
	s_cbranch_scc1 .Lsf14_skip
	v_mov_b32_e32 v8, 0x20020
	ds_read_b32 v9, v8 offset:4
	v_mbcnt_lo_u32_b32 v2, -1, 0
	v_mbcnt_hi_u32_b32 v2, -1, v2
	v_readlane_b32 s6, v247, 0
	v_readlane_b32 s7, v247, 1
	s_load_dword s38, s[6:7], 0xe8
	v_readlane_b32 s39, v247, 6
	s_waitcnt lgkmcnt(0)
	v_readfirstlane_b32 s5, v9
	s_mov_b32 s37, 0
	s_cmp_ge_u32 s5, 112
	s_cbranch_scc0 .Lsf14_go
	s_mov_b32 s37, 1
	s_add_i32 s5, s39, s38
	s_cmpk_ge_u32 s5, 0x100
	s_cbranch_scc1 .Lsf14_skip
.Lsf14_go:
	s_add_i32 s5, s4, -1
	s_lshl_b32 s5, s5, 14
	v_lshl_add_u32 v7, v2, 4, s5
	ds_write_b128 v7, v[160:163] offset:0
	ds_write_b128 v7, v[164:167] offset:1024
	ds_write_b128 v7, v[168:171] offset:2048
	ds_write_b128 v7, v[172:175] offset:3072
	ds_write_b128 v7, v[176:179] offset:4096
	ds_write_b128 v7, v[180:183] offset:5120
	ds_write_b128 v7, v[184:187] offset:6144
	ds_write_b128 v7, v[188:191] offset:7168
	ds_write_b128 v7, v[192:195] offset:8192
	ds_write_b128 v7, v[196:199] offset:9216
	ds_write_b128 v7, v[200:203] offset:10240
	ds_write_b128 v7, v[204:207] offset:11264
	ds_write_b128 v7, v[208:211] offset:12288
	ds_write_b128 v7, v[212:215] offset:13312
	ds_write_b128 v7, v[216:219] offset:14336
	ds_write_b128 v7, v[220:223] offset:15360
	v_readlane_b32 s6, v247, 0
	v_readlane_b32 s7, v247, 1
	s_load_dwordx2 s[10:11], s[6:7], 0xc0
	s_load_dwordx2 s[12:13], s[6:7], 0xc8
	v_readlane_b32 s33, v247, 6
	v_mov_b32_e32 v3, 0x43e00000
	v_cmp_eq_u32_e32 vcc, 0, v2
	s_mul_i32 s33, s33, 112
	s_nop 1
	v_cndmask_b32_e64 v18, 0, 1, vcc
	s_waitcnt lgkmcnt(0)
.Lsf14_loop:
	s_cmp_eq_u32 s37, 0
	s_cbranch_scc0 .Lsf14_orph
	ds_add_rtn_u32 v9, v8, v18 offset:4
	s_waitcnt lgkmcnt(0)
	v_readfirstlane_b32 s18, v9
	s_cmp_ge_u32 s18, 112
	s_cbranch_scc0 .Lsf14_own
	s_mov_b32 s37, 1
	s_branch .Lsf14_loop

; __device__ __forceinline__ void moe_convert(Frame& F, int lo, int hi, int rank, int nrank) {
;     ...
;     for (int it = lo + rank; it < hi; it += nrank) {
;         int r = it; const float* W; unsigned char* WT; int N, ldt, kind, off; float f8s;
;         if (r < 14336) { const int e = r / 1792; r -= e * 1792; W = F.in[IN_WMG] + (size_t)e * 2048 * DFFE; N = DFFE; WT = F.ws + WS_WGU1 + (size_t)e * 14336 * 2048; ldt = 2048; kind = 1; off = 0; f8s = 32.f; }
;         else if ((r -= 14336) < 14336) { const int e = r / 1792; r -= e * 1792; W = F.in[IN_WMU] + (size_t)e * 2048 * DFFE; N = DFFE; WT = F.ws + WS_WGU1 + (size_t)e * 14336 * 2048; ldt = 2048; kind = 1; off = 128; f8s = 256.f; }
;         else { r -= 14336; const int e = r / 1792; r -= e * 1792; W = F.in[IN_WMD] + (size_t)e * DFFE * 2048; N = 2048; WT = F.ws + WS_WDN1 + (size_t)e * 2048 * DFFE; ldt = DFFE; kind = 0; off = 0; f8s = 64.f; }
.Lsf14_orph:
	ds_add_rtn_u32 v9, v8, v18 offset:8
	s_waitcnt lgkmcnt(0)
	v_readfirstlane_b32 s18, v9
	s_mul_hi_u32 s35, s18, 0x2492493
	s_mul_i32 s36, s35, 112
	s_sub_i32 s36, s18, s36
	s_add_i32 s35, s35, 1
	s_mul_i32 s35, s35, s38
	s_add_i32 s35, s35, s39
	s_cmpk_ge_u32 s35, 0x100
	s_cbranch_scc1 .Lsf14_done
	s_mul_i32 s35, s35, 112
	s_add_i32 s18, s35, s36
.Lsf14_unit:
	s_and_b32 s27, s18, 1
	s_lshr_b32 s19, s18, 1
	s_add_i32 s19, s19, 0x5000
	s_cmp_lt_u32 s19, 0x7000
	s_cbranch_scc0 .Lsf14_down
	s_add_i32 s20, s19, 0xffffc800
	s_lshr_b32 s21, s20, 8
	s_mul_i32 s21, s21, 37
	s_lshr_b32 s21, s21, 8
	s_mul_i32 s28, s21, 0x700
	s_sub_i32 s20, s20, s28
	s_mul_i32 s28, s21, 0x3800000
	s_add_u32 s14, s10, s28
	s_addc_u32 s15, s11, 0
	s_mul_i32 s28, s21, 0x1c00000
	s_add_u32 s28, s28, 0x7800000
	s_add_u32 s16, s86, s28
	s_addc_u32 s17, s87, 0
	s_movk_i32 s24, 0x7000
	s_movk_i32 s25, 0x800
	s_mov_b32 s26, 0x43800000
	s_lshr_b32 s22, s20, 4
	s_mul_i32 s22, s22, 0x2493
	s_lshr_b32 s22, s22, 16
	s_mul_i32 s28, s22, 0x70
	s_sub_i32 s23, s20, s28
	s_mov_b32 s29, 1
	s_branch .Lsf14_dec
